# grid barrier leader path: dropped two waits (before the acquire invalidate, and after the generation release add) that only delayed the last-arriving workgroup
# speedup vs baseline: 1.0061x; 1.0041x over previous
; __device__ __forceinline__ unsigned xb_ld(unsigned* p)              { return __hip_atomic_load(p, __ATOMIC_RELAXED, __HIP_MEMORY_SCOPE_AGENT); }
; __device__ __forceinline__ unsigned xb_add(unsigned* p, unsigned v) { return __hip_atomic_fetch_add(p, v, __ATOMIC_RELAXED, __HIP_MEMORY_SCOPE_AGENT); }
; #define XB_SPIN(cond, bar) do { unsigned _sp = 0; while (cond) { __builtin_amdgcn_s_sleep(1); \
;     if ((++_sp & 255u) == 0u) { if (xb_ld(&(bar)[XB_TMO])) break; if (_sp > XB_SPIN_CAP) { atomicAdd(&(bar)[XB_TMO], 1u); break; } } } } while (0)
; __device__ __forceinline__ void xcd_barrier(const XcdBarrier& b) {
;     ...
;             __builtin_amdgcn_fence(__ATOMIC_RELEASE, "agent");
;             asm volatile("s_waitcnt vmcnt(0)" ::: "memory");
;             const unsigned og = xb_add(&bar[XB_TOP], 1u);
;             const unsigned tg = og / nx;
;             if (og + 1u == (tg + 1u) * nx) xb_add(&bar[XB_TOPGEN], 1u);
;             else XB_SPIN(xb_ld(&bar[XB_TOPGEN]) == tg, bar);
;             __builtin_amdgcn_fence(__ATOMIC_ACQUIRE, "agent");
;             asm volatile("s_waitcnt vmcnt(0)" ::: "memory");
;             xb_add(&bar[XB_XGEN(b.x)], 1u);
;             asm volatile("s_waitcnt vmcnt(0)" ::: "memory");
;         } else {
;             XB_SPIN(xb_ld(&bar[XB_XGEN(b.x)]) == gen, bar);
;             asm volatile("buffer_inv sc0\n\ts_waitcnt vmcnt(0)" ::: "memory");
;         }
;     }
;     __syncthreads();
.LBB0_76:
	s_or_b64 exec, exec, s[8:9]
	s_mov_b64 s[8:9], exec
	buffer_inv sc1
	s_waitcnt vmcnt(0)
	v_mbcnt_lo_u32_b32 v2, s8, 0
	v_mbcnt_hi_u32_b32 v2, s9, v2
	v_cmp_eq_u32_e32 vcc, 0, v2
	s_and_saveexec_b64 s[10:11], vcc
	s_cbranch_execz .LBB0_78
	s_bcnt1_i32_b64 s2, s[8:9]
	v_mov_b32_e32 v2, 0x2000
	v_mov_b32_e32 v3, s2
	global_atomic_add v2, v3, s[6:7] offset:1024
.LBB0_78:
	s_or_b64 exec, exec, s[10:11]
.LBB0_79:
	s_or_b64 exec, exec, s[4:5]
	s_waitcnt lgkmcnt(0)
	s_barrier

; __device__ __forceinline__ unsigned xb_ld(unsigned* p)              { return __hip_atomic_load(p, __ATOMIC_RELAXED, __HIP_MEMORY_SCOPE_AGENT); }
; __device__ __forceinline__ unsigned xb_add(unsigned* p, unsigned v) { return __hip_atomic_fetch_add(p, v, __ATOMIC_RELAXED, __HIP_MEMORY_SCOPE_AGENT); }
; #define XB_SPIN(cond, bar) do { unsigned _sp = 0; while (cond) { __builtin_amdgcn_s_sleep(1); \
;     if ((++_sp & 255u) == 0u) { if (xb_ld(&(bar)[XB_TMO])) break; if (_sp > XB_SPIN_CAP) { atomicAdd(&(bar)[XB_TMO], 1u); break; } } } } while (0)
; __device__ __forceinline__ void xcd_barrier(const XcdBarrier& b) {
;     ...
;             __builtin_amdgcn_fence(__ATOMIC_RELEASE, "agent");
;             asm volatile("s_waitcnt vmcnt(0)" ::: "memory");
;             const unsigned og = xb_add(&bar[XB_TOP], 1u);
;             const unsigned tg = og / nx;
;             if (og + 1u == (tg + 1u) * nx) xb_add(&bar[XB_TOPGEN], 1u);
;             else XB_SPIN(xb_ld(&bar[XB_TOPGEN]) == tg, bar);
;             __builtin_amdgcn_fence(__ATOMIC_ACQUIRE, "agent");
;             asm volatile("s_waitcnt vmcnt(0)" ::: "memory");
;             xb_add(&bar[XB_XGEN(b.x)], 1u);
;             asm volatile("s_waitcnt vmcnt(0)" ::: "memory");
;         } else {
;             XB_SPIN(xb_ld(&bar[XB_XGEN(b.x)]) == gen, bar);
;             asm volatile("buffer_inv sc0\n\ts_waitcnt vmcnt(0)" ::: "memory");
;         }
;     }
;     __syncthreads();
.LBB0_334:
	s_or_b64 exec, exec, s[10:11]
.LBB0_335:
	s_or_b64 exec, exec, s[0:1]
	s_waitcnt lgkmcnt(0)
	s_barrier

; __device__ __forceinline__ unsigned xb_ld(unsigned* p)              { return __hip_atomic_load(p, __ATOMIC_RELAXED, __HIP_MEMORY_SCOPE_AGENT); }
; __device__ __forceinline__ unsigned xb_add(unsigned* p, unsigned v) { return __hip_atomic_fetch_add(p, v, __ATOMIC_RELAXED, __HIP_MEMORY_SCOPE_AGENT); }
; #define XB_SPIN(cond, bar) do { unsigned _sp = 0; while (cond) { __builtin_amdgcn_s_sleep(1); \
;     if ((++_sp & 255u) == 0u) { if (xb_ld(&(bar)[XB_TMO])) break; if (_sp > XB_SPIN_CAP) { atomicAdd(&(bar)[XB_TMO], 1u); break; } } } } while (0)
; __device__ __forceinline__ void xcd_barrier(const XcdBarrier& b) {
;     ...
;             __builtin_amdgcn_fence(__ATOMIC_RELEASE, "agent");
;             asm volatile("s_waitcnt vmcnt(0)" ::: "memory");
;             const unsigned og = xb_add(&bar[XB_TOP], 1u);
;             const unsigned tg = og / nx;
;             if (og + 1u == (tg + 1u) * nx) xb_add(&bar[XB_TOPGEN], 1u);
;             else XB_SPIN(xb_ld(&bar[XB_TOPGEN]) == tg, bar);
;             __builtin_amdgcn_fence(__ATOMIC_ACQUIRE, "agent");
;             asm volatile("s_waitcnt vmcnt(0)" ::: "memory");
;             xb_add(&bar[XB_XGEN(b.x)], 1u);
;             asm volatile("s_waitcnt vmcnt(0)" ::: "memory");
;         } else {
;             XB_SPIN(xb_ld(&bar[XB_XGEN(b.x)]) == gen, bar);
;             asm volatile("buffer_inv sc0\n\ts_waitcnt vmcnt(0)" ::: "memory");
;         }
;     }
;     __syncthreads();
.LBB0_474:
	s_or_b64 exec, exec, s[10:11]
.LBB0_475:
	s_or_b64 exec, exec, s[4:5]
	s_waitcnt lgkmcnt(0)
	s_barrier

; __device__ __forceinline__ unsigned xb_ld(unsigned* p)              { return __hip_atomic_load(p, __ATOMIC_RELAXED, __HIP_MEMORY_SCOPE_AGENT); }
; __device__ __forceinline__ unsigned xb_add(unsigned* p, unsigned v) { return __hip_atomic_fetch_add(p, v, __ATOMIC_RELAXED, __HIP_MEMORY_SCOPE_AGENT); }
; #define XB_SPIN(cond, bar) do { unsigned _sp = 0; while (cond) { __builtin_amdgcn_s_sleep(1); \
;     if ((++_sp & 255u) == 0u) { if (xb_ld(&(bar)[XB_TMO])) break; if (_sp > XB_SPIN_CAP) { atomicAdd(&(bar)[XB_TMO], 1u); break; } } } } while (0)
; __device__ __forceinline__ void xcd_barrier(const XcdBarrier& b) {
;     ...
;             __builtin_amdgcn_fence(__ATOMIC_RELEASE, "agent");
;             asm volatile("s_waitcnt vmcnt(0)" ::: "memory");
;             const unsigned og = xb_add(&bar[XB_TOP], 1u);
;             const unsigned tg = og / nx;
;             if (og + 1u == (tg + 1u) * nx) xb_add(&bar[XB_TOPGEN], 1u);
;             else XB_SPIN(xb_ld(&bar[XB_TOPGEN]) == tg, bar);
;             __builtin_amdgcn_fence(__ATOMIC_ACQUIRE, "agent");
;             asm volatile("s_waitcnt vmcnt(0)" ::: "memory");
;             xb_add(&bar[XB_XGEN(b.x)], 1u);
;             asm volatile("s_waitcnt vmcnt(0)" ::: "memory");
;         } else {
;             XB_SPIN(xb_ld(&bar[XB_XGEN(b.x)]) == gen, bar);
;             asm volatile("buffer_inv sc0\n\ts_waitcnt vmcnt(0)" ::: "memory");
;         }
;     }
;     __syncthreads();
.LBB0_539:
	s_or_b64 exec, exec, s[10:11]
.LBB0_540:
	s_or_b64 exec, exec, s[4:5]
	s_waitcnt lgkmcnt(0)
	s_barrier

; __device__ __forceinline__ unsigned xb_ld(unsigned* p)              { return __hip_atomic_load(p, __ATOMIC_RELAXED, __HIP_MEMORY_SCOPE_AGENT); }
; __device__ __forceinline__ unsigned xb_add(unsigned* p, unsigned v) { return __hip_atomic_fetch_add(p, v, __ATOMIC_RELAXED, __HIP_MEMORY_SCOPE_AGENT); }
; #define XB_SPIN(cond, bar) do { unsigned _sp = 0; while (cond) { __builtin_amdgcn_s_sleep(1); \
;     if ((++_sp & 255u) == 0u) { if (xb_ld(&(bar)[XB_TMO])) break; if (_sp > XB_SPIN_CAP) { atomicAdd(&(bar)[XB_TMO], 1u); break; } } } } while (0)
; __device__ __forceinline__ void xcd_barrier(const XcdBarrier& b) {
;     ...
;             __builtin_amdgcn_fence(__ATOMIC_RELEASE, "agent");
;             asm volatile("s_waitcnt vmcnt(0)" ::: "memory");
;             const unsigned og = xb_add(&bar[XB_TOP], 1u);
;             const unsigned tg = og / nx;
;             if (og + 1u == (tg + 1u) * nx) xb_add(&bar[XB_TOPGEN], 1u);
;             else XB_SPIN(xb_ld(&bar[XB_TOPGEN]) == tg, bar);
;             __builtin_amdgcn_fence(__ATOMIC_ACQUIRE, "agent");
;             asm volatile("s_waitcnt vmcnt(0)" ::: "memory");
;             xb_add(&bar[XB_XGEN(b.x)], 1u);
;             asm volatile("s_waitcnt vmcnt(0)" ::: "memory");
;         } else {
;             XB_SPIN(xb_ld(&bar[XB_XGEN(b.x)]) == gen, bar);
;             asm volatile("buffer_inv sc0\n\ts_waitcnt vmcnt(0)" ::: "memory");
;         }
;     }
;     __syncthreads();
.LBB0_598:
	s_or_b64 exec, exec, s[10:11]
.LBB0_599:
	s_or_b64 exec, exec, s[4:5]
	s_waitcnt lgkmcnt(0)
	s_barrier

; __device__ __forceinline__ unsigned xb_ld(unsigned* p)              { return __hip_atomic_load(p, __ATOMIC_RELAXED, __HIP_MEMORY_SCOPE_AGENT); }
; __device__ __forceinline__ unsigned xb_add(unsigned* p, unsigned v) { return __hip_atomic_fetch_add(p, v, __ATOMIC_RELAXED, __HIP_MEMORY_SCOPE_AGENT); }
; #define XB_SPIN(cond, bar) do { unsigned _sp = 0; while (cond) { __builtin_amdgcn_s_sleep(1); \
;     if ((++_sp & 255u) == 0u) { if (xb_ld(&(bar)[XB_TMO])) break; if (_sp > XB_SPIN_CAP) { atomicAdd(&(bar)[XB_TMO], 1u); break; } } } } while (0)
; __device__ __forceinline__ void xcd_barrier(const XcdBarrier& b) {
;     ...
;             __builtin_amdgcn_fence(__ATOMIC_RELEASE, "agent");
;             asm volatile("s_waitcnt vmcnt(0)" ::: "memory");
;             const unsigned og = xb_add(&bar[XB_TOP], 1u);
;             const unsigned tg = og / nx;
;             if (og + 1u == (tg + 1u) * nx) xb_add(&bar[XB_TOPGEN], 1u);
;             else XB_SPIN(xb_ld(&bar[XB_TOPGEN]) == tg, bar);
;             __builtin_amdgcn_fence(__ATOMIC_ACQUIRE, "agent");
;             asm volatile("s_waitcnt vmcnt(0)" ::: "memory");
;             xb_add(&bar[XB_XGEN(b.x)], 1u);
;             asm volatile("s_waitcnt vmcnt(0)" ::: "memory");
;         } else {
;             XB_SPIN(xb_ld(&bar[XB_XGEN(b.x)]) == gen, bar);
;             asm volatile("buffer_inv sc0\n\ts_waitcnt vmcnt(0)" ::: "memory");
;         }
;     }
;     __syncthreads();
.LBB0_676:
	s_or_b64 exec, exec, s[6:7]
	s_mov_b64 s[6:7], exec
	buffer_inv sc1
	s_waitcnt vmcnt(0)
	v_mbcnt_lo_u32_b32 v2, s6, 0
	v_mbcnt_hi_u32_b32 v2, s7, v2
	v_cmp_eq_u32_e32 vcc, 0, v2
	s_and_saveexec_b64 s[8:9], vcc
	s_cbranch_execz .LBB0_678
	s_bcnt1_i32_b64 s6, s[6:7]
	v_mov_b32_e32 v2, 0x2000
	v_mov_b32_e32 v3, s6
	global_atomic_add v2, v3, s[4:5] offset:1024
.LBB0_678:
	s_or_b64 exec, exec, s[8:9]
.LBB0_679:
	s_or_b64 exec, exec, s[0:1]
	s_waitcnt lgkmcnt(0)
	s_barrier

; __device__ __forceinline__ unsigned xb_ld(unsigned* p)              { return __hip_atomic_load(p, __ATOMIC_RELAXED, __HIP_MEMORY_SCOPE_AGENT); }
; __device__ __forceinline__ unsigned xb_add(unsigned* p, unsigned v) { return __hip_atomic_fetch_add(p, v, __ATOMIC_RELAXED, __HIP_MEMORY_SCOPE_AGENT); }
; #define XB_SPIN(cond, bar) do { unsigned _sp = 0; while (cond) { __builtin_amdgcn_s_sleep(1); \
;     if ((++_sp & 255u) == 0u) { if (xb_ld(&(bar)[XB_TMO])) break; if (_sp > XB_SPIN_CAP) { atomicAdd(&(bar)[XB_TMO], 1u); break; } } } } while (0)
; __device__ __forceinline__ void xcd_barrier(const XcdBarrier& b) {
;     ...
;             __builtin_amdgcn_fence(__ATOMIC_RELEASE, "agent");
;             asm volatile("s_waitcnt vmcnt(0)" ::: "memory");
;             const unsigned og = xb_add(&bar[XB_TOP], 1u);
;             const unsigned tg = og / nx;
;             if (og + 1u == (tg + 1u) * nx) xb_add(&bar[XB_TOPGEN], 1u);
;             else XB_SPIN(xb_ld(&bar[XB_TOPGEN]) == tg, bar);
;             __builtin_amdgcn_fence(__ATOMIC_ACQUIRE, "agent");
;             asm volatile("s_waitcnt vmcnt(0)" ::: "memory");
;             xb_add(&bar[XB_XGEN(b.x)], 1u);
;             asm volatile("s_waitcnt vmcnt(0)" ::: "memory");
;         } else {
;             XB_SPIN(xb_ld(&bar[XB_XGEN(b.x)]) == gen, bar);
;             asm volatile("buffer_inv sc0\n\ts_waitcnt vmcnt(0)" ::: "memory");
;         }
;     }
;     __syncthreads();
.LBB0_756:
	s_or_b64 exec, exec, s[6:7]
	s_mov_b64 s[6:7], exec
	buffer_inv sc1
	s_waitcnt vmcnt(0)
	v_mbcnt_lo_u32_b32 v1, s6, 0
	v_mbcnt_hi_u32_b32 v1, s7, v1
	v_cmp_eq_u32_e32 vcc, 0, v1
	s_and_saveexec_b64 s[8:9], vcc
	s_cbranch_execz .LBB0_758
	s_bcnt1_i32_b64 s6, s[6:7]
	v_mov_b32_e32 v1, 0x2000
	v_mov_b32_e32 v2, s6
	global_atomic_add v1, v2, s[4:5] offset:1024
.LBB0_758:
	s_or_b64 exec, exec, s[8:9]
.LBB0_759:
	s_or_b64 exec, exec, s[0:1]
	s_waitcnt lgkmcnt(0)
	s_barrier

; __device__ __forceinline__ unsigned xb_ld(unsigned* p)              { return __hip_atomic_load(p, __ATOMIC_RELAXED, __HIP_MEMORY_SCOPE_AGENT); }
; __device__ __forceinline__ unsigned xb_add(unsigned* p, unsigned v) { return __hip_atomic_fetch_add(p, v, __ATOMIC_RELAXED, __HIP_MEMORY_SCOPE_AGENT); }
; #define XB_SPIN(cond, bar) do { unsigned _sp = 0; while (cond) { __builtin_amdgcn_s_sleep(1); \
;     if ((++_sp & 255u) == 0u) { if (xb_ld(&(bar)[XB_TMO])) break; if (_sp > XB_SPIN_CAP) { atomicAdd(&(bar)[XB_TMO], 1u); break; } } } } while (0)
; __device__ __forceinline__ void xcd_barrier(const XcdBarrier& b) {
;     ...
;             __builtin_amdgcn_fence(__ATOMIC_RELEASE, "agent");
;             asm volatile("s_waitcnt vmcnt(0)" ::: "memory");
;             const unsigned og = xb_add(&bar[XB_TOP], 1u);
;             const unsigned tg = og / nx;
;             if (og + 1u == (tg + 1u) * nx) xb_add(&bar[XB_TOPGEN], 1u);
;             else XB_SPIN(xb_ld(&bar[XB_TOPGEN]) == tg, bar);
;             __builtin_amdgcn_fence(__ATOMIC_ACQUIRE, "agent");
;             asm volatile("s_waitcnt vmcnt(0)" ::: "memory");
;             xb_add(&bar[XB_XGEN(b.x)], 1u);
;             asm volatile("s_waitcnt vmcnt(0)" ::: "memory");
;         } else {
;             XB_SPIN(xb_ld(&bar[XB_XGEN(b.x)]) == gen, bar);
;             asm volatile("buffer_inv sc0\n\ts_waitcnt vmcnt(0)" ::: "memory");
;         }
;     }
;     __syncthreads();
.LBB0_1184:
	s_or_b64 exec, exec, s[8:9]
.LBB0_1185:
	s_or_b64 exec, exec, s[2:3]
	s_waitcnt lgkmcnt(0)
	s_barrier

; __device__ __forceinline__ unsigned xb_ld(unsigned* p)              { return __hip_atomic_load(p, __ATOMIC_RELAXED, __HIP_MEMORY_SCOPE_AGENT); }
; __device__ __forceinline__ unsigned xb_add(unsigned* p, unsigned v) { return __hip_atomic_fetch_add(p, v, __ATOMIC_RELAXED, __HIP_MEMORY_SCOPE_AGENT); }
; #define XB_SPIN(cond, bar) do { unsigned _sp = 0; while (cond) { __builtin_amdgcn_s_sleep(1); \
;     if ((++_sp & 255u) == 0u) { if (xb_ld(&(bar)[XB_TMO])) break; if (_sp > XB_SPIN_CAP) { atomicAdd(&(bar)[XB_TMO], 1u); break; } } } } while (0)
; __device__ __forceinline__ void xcd_barrier(const XcdBarrier& b) {
;     ...
;             __builtin_amdgcn_fence(__ATOMIC_RELEASE, "agent");
;             asm volatile("s_waitcnt vmcnt(0)" ::: "memory");
;             const unsigned og = xb_add(&bar[XB_TOP], 1u);
;             const unsigned tg = og / nx;
;             if (og + 1u == (tg + 1u) * nx) xb_add(&bar[XB_TOPGEN], 1u);
;             else XB_SPIN(xb_ld(&bar[XB_TOPGEN]) == tg, bar);
;             __builtin_amdgcn_fence(__ATOMIC_ACQUIRE, "agent");
;             asm volatile("s_waitcnt vmcnt(0)" ::: "memory");
;             xb_add(&bar[XB_XGEN(b.x)], 1u);
;             asm volatile("s_waitcnt vmcnt(0)" ::: "memory");
;         } else {
;             XB_SPIN(xb_ld(&bar[XB_XGEN(b.x)]) == gen, bar);
;             asm volatile("buffer_inv sc0\n\ts_waitcnt vmcnt(0)" ::: "memory");
;         }
;     }
;     __syncthreads();
.LBB0_1636:
	s_or_b64 exec, exec, s[8:9]
.LBB0_1637:
	s_or_b64 exec, exec, s[2:3]
	s_waitcnt lgkmcnt(0)
	s_barrier
